# speedup vs baseline: 1.0381x; 1.0230x over previous
.Lp1_fin:
	s_lshl_b64 s[0:1], s[20:21], 1
	s_add_u32 s0, s18, s0
	s_addc_u32 s1, s19, s1
	global_load_dwordx4 v[2:5], v[66:67], off
	global_load_dwordx4 v[6:9], v[68:69], off
	v_lshlrev_b32_e32 v10, 1, v79
	global_load_dwordx4 v[10:13], v10, s[0:1]
	v_lshlrev_b32_e32 v14, 1, v80
	global_load_dwordx4 v[14:17], v14, s[0:1]
	v_mov_b32_e32 v200, 0
	v_mov_b32_e32 v201, 0
	v_mov_b32_e32 v202, 0
	v_mov_b32_e32 v83, 0
	v_exp_f32_e32 v34, v34
	v_exp_f32_e32 v35, v35
	v_add_f32_e32 v200, v200, v34
	v_exp_f32_e32 v36, v36
	v_add_f32_e32 v201, v201, v35
	v_exp_f32_e32 v37, v37
	v_add_f32_e32 v202, v202, v36
	v_exp_f32_e32 v38, v38
	v_add_f32_e32 v83, v83, v37
	v_exp_f32_e32 v39, v39
	v_add_f32_e32 v200, v200, v38
	v_exp_f32_e32 v40, v40
	v_add_f32_e32 v201, v201, v39
	v_exp_f32_e32 v41, v41
	v_add_f32_e32 v202, v202, v40
	v_exp_f32_e32 v42, v42
	v_add_f32_e32 v83, v83, v41
	v_exp_f32_e32 v43, v43
	v_add_f32_e32 v200, v200, v42
	v_exp_f32_e32 v44, v44
	v_add_f32_e32 v201, v201, v43
	v_exp_f32_e32 v45, v45
	v_add_f32_e32 v202, v202, v44
	v_exp_f32_e32 v46, v46
	v_add_f32_e32 v83, v83, v45
	v_exp_f32_e32 v47, v47
	v_add_f32_e32 v200, v200, v46
	v_exp_f32_e32 v48, v48
	v_add_f32_e32 v201, v201, v47
	v_exp_f32_e32 v49, v49
	v_add_f32_e32 v202, v202, v48
	v_exp_f32_e32 v50, v50
	v_add_f32_e32 v83, v83, v49
	v_exp_f32_e32 v51, v51
	v_add_f32_e32 v200, v200, v50
	v_exp_f32_e32 v52, v52
	v_add_f32_e32 v201, v201, v51
	v_exp_f32_e32 v53, v53
	v_add_f32_e32 v202, v202, v52
	v_exp_f32_e32 v54, v54
	v_add_f32_e32 v83, v83, v53
	v_exp_f32_e32 v55, v55
	v_add_f32_e32 v200, v200, v54
	v_exp_f32_e32 v56, v56
	v_add_f32_e32 v201, v201, v55
	v_exp_f32_e32 v57, v57
	v_add_f32_e32 v202, v202, v56
	v_exp_f32_e32 v58, v58
	v_add_f32_e32 v83, v83, v57
	v_exp_f32_e32 v59, v59
	v_add_f32_e32 v200, v200, v58
	v_exp_f32_e32 v60, v60
	v_add_f32_e32 v201, v201, v59
	v_exp_f32_e32 v61, v61
	v_add_f32_e32 v202, v202, v60
	v_exp_f32_e32 v62, v62
	v_add_f32_e32 v83, v83, v61
	v_exp_f32_e32 v63, v63
	v_add_f32_e32 v200, v200, v62
	v_exp_f32_e32 v64, v64
	v_add_f32_e32 v201, v201, v63
	v_exp_f32_e32 v65, v65
	v_add_f32_e32 v202, v202, v64
	v_add_f32_e32 v83, v83, v65
	v_add_f32_e32 v200, v200, v201
	v_add_f32_e32 v202, v202, v83
	v_add_f32_e32 v200, v200, v202
	v_add_f32_e32 v82, v82, v200
	s_barrier
	v_mbcnt_lo_u32_b32 v21, -1, 0
	v_mbcnt_hi_u32_b32 v21, -1, v21
	v_and_b32_e32 v23, 64, v21
	v_xor_b32_e32 v22, 32, v21
	v_add_u32_e32 v24, 64, v23
	v_cmp_lt_i32_e32 vcc, v22, v24
	v_cndmask_b32_e32 v21, v21, v22, vcc
	v_lshlrev_b32_e32 v21, 2, v21
	ds_bpermute_b32 v22, v21, v81
	v_mov_b32_e32 v18, v82
	ds_bpermute_b32 v19, v21, v18
	v_max_f32_e32 v21, v81, v81
	s_mov_b32 s15, 0
	s_waitcnt lgkmcnt(1)
	v_max_f32_e32 v20, v22, v22
	v_max_f32_e32 v20, v21, v20
	v_sub_f32_e32 v22, v22, v20
	v_sub_f32_e32 v21, v81, v20
	v_exp_f32_e32 v22, v22
	v_exp_f32_e32 v21, v21
	s_lshl_b64 s[18:19], s[14:15], 18
	v_mov_b32_e32 v131, 0
	s_waitcnt lgkmcnt(0)
	v_mul_f32_e32 v19, v22, v19
	v_fmac_f32_e32 v19, v18, v21
	v_div_scale_f32 v18, s[10:11], v19, v19, 1.0
	s_movk_i32 s10, 0x60
	s_nop 0
	v_mad_u32_u24 v188, v73, s10, v74
	v_mad_u32_u24 v189, v75, s10, v74
	s_waitcnt vmcnt(3)
	ds_write_b128 v77, v[2:5]
	s_waitcnt vmcnt(2)
	ds_write_b128 v78, v[6:9]
	v_lshlrev_b32_e32 v2, 1, v188
	s_waitcnt vmcnt(1)
	ds_write_b128 v2, v[10:13]
	v_lshlrev_b32_e32 v2, 1, v189
	s_mul_i32 s10, s14, 0x1200
	s_waitcnt vmcnt(0)
	ds_write_b128 v2, v[14:17]
	s_add_i32 s10, s10, 0xa800
	v_lshrrev_b32_e32 v2, 2, v0
	v_and_or_b32 v3, v2, 3, v1
	s_movk_i32 s11, 0x48
	v_mov_b32_e32 v5, s10
	v_add_u32_e32 v4, s10, v76
	v_mad_u32_u24 v5, v3, s11, v5
	s_lshl_b64 s[10:11], s[12:13], 24
	s_and_b32 s13, s2, 15
	s_lshl_b32 s13, s13, 20
	v_and_b32_e32 v0, 3, v0
	s_or_b32 s10, s10, s13
	v_and_or_b32 v0, v2, 4, v0
	s_add_u32 s10, s10, s18
	v_lshlrev_b32_e32 v0, 3, v0
	v_mul_u32_u24_e32 v2, 0xc0, v3
	v_lshlrev_b32_e32 v3, 13, v72
	s_addc_u32 s11, s11, s19
	v_or_b32_e32 v185, v2, v0
	v_or_b32_e32 v2, v3, v164
	s_add_u32 s10, s4, s10
	v_lshlrev_b32_e32 v130, 2, v2
	s_addc_u32 s11, s5, s11
	v_lshl_add_u64 v[2:3], s[10:11], 0, v[130:131]
	s_mov_b64 s[18:19], 0x80
	v_lshl_add_u64 v[132:133], v[2:3], 0, s[18:19]
	v_or_b32_e32 v2, 0x36000, v130
	v_mov_b32_e32 v3, v131
	v_lshl_add_u64 v[134:135], s[10:11], 0, v[2:3]
	v_or_b32_e32 v2, 0x2000, v130
	v_lshl_add_u64 v[2:3], s[10:11], 0, v[2:3]
	v_lshl_add_u64 v[136:137], v[2:3], 0, s[18:19]
	v_or_b32_e32 v2, 0x34000, v130
	v_mov_b32_e32 v3, v131
	v_rcp_f32_e32 v21, v18
	v_lshl_add_u64 v[138:139], s[10:11], 0, v[2:3]
	v_or_b32_e32 v2, 0x4000, v130
	v_lshl_add_u64 v[2:3], s[10:11], 0, v[2:3]
	v_lshl_add_u64 v[140:141], v[2:3], 0, s[18:19]
	v_or_b32_e32 v2, 0x32000, v130
	v_mov_b32_e32 v3, v131
	v_lshl_add_u64 v[142:143], s[10:11], 0, v[2:3]
	v_or_b32_e32 v2, 0x6000, v130
	v_fma_f32 v22, -v18, v21, 1.0
	v_lshl_add_u64 v[2:3], s[10:11], 0, v[2:3]
	v_fmac_f32_e32 v21, v22, v21
	v_div_scale_f32 v22, vcc, 1.0, v19, 1.0
	v_lshl_add_u64 v[144:145], v[2:3], 0, s[18:19]
	v_or_b32_e32 v2, 0x30000, v130
	v_mov_b32_e32 v3, v131
	v_mul_f32_e32 v24, v22, v21
	v_lshl_add_u64 v[146:147], s[10:11], 0, v[2:3]
	v_or_b32_e32 v2, 0x10000, v130
	v_fma_f32 v25, -v18, v24, v22
	v_lshl_add_u64 v[2:3], s[10:11], 0, v[2:3]
	v_fmac_f32_e32 v24, v25, v21
	v_lshl_add_u64 v[148:149], v[2:3], 0, s[18:19]
	v_or_b32_e32 v2, 0x26000, v130
	v_mov_b32_e32 v3, v131
	v_fma_f32 v18, -v18, v24, v22
	v_lshl_add_u64 v[150:151], s[10:11], 0, v[2:3]
	v_or_b32_e32 v2, 0x12000, v130
	v_div_fmas_f32 v18, v18, v21, v24
	v_lshlrev_b32_e32 v184, 2, v72
	v_lshl_add_u64 v[2:3], s[10:11], 0, v[2:3]
	v_div_fixup_f32 v18, v18, v19, 1.0
	v_or_b32_e32 v19, v184, v23
	v_lshl_add_u64 v[152:153], v[2:3], 0, s[18:19]
	v_or_b32_e32 v2, 0x24000, v130
	v_mov_b32_e32 v3, v131
	v_lshlrev_b32_e32 v19, 2, v19
	v_lshl_add_u64 v[154:155], s[10:11], 0, v[2:3]
	v_or_b32_e32 v2, 0x14000, v130
	ds_bpermute_b32 v33, v19, v20 offset:36
	ds_bpermute_b32 v32, v19, v20 offset:40
	ds_bpermute_b32 v35, v19, v20 offset:44
	ds_bpermute_b32 v34, v19, v20 offset:64
	ds_bpermute_b32 v37, v19, v20 offset:68
	ds_bpermute_b32 v36, v19, v20 offset:72
	ds_bpermute_b32 v39, v19, v20 offset:76
	ds_bpermute_b32 v38, v19, v20 offset:96
	ds_bpermute_b32 v41, v19, v20 offset:100
	ds_bpermute_b32 v40, v19, v20 offset:104
	ds_bpermute_b32 v43, v19, v20 offset:108
	v_lshl_add_u64 v[2:3], s[10:11], 0, v[2:3]
	ds_bpermute_b32 v46, v19, v20 offset:32
	ds_bpermute_b32 v47, v19, v20 offset:12
	ds_bpermute_b32 v42, v19, v20 offset:8
	ds_bpermute_b32 v45, v19, v20 offset:4
	ds_bpermute_b32 v44, v19, v20
	ds_bpermute_b32 v183, v19, v18
	ds_bpermute_b32 v182, v19, v18 offset:4
	ds_bpermute_b32 v181, v19, v18 offset:8
	ds_bpermute_b32 v180, v19, v18 offset:12
	ds_bpermute_b32 v179, v19, v18 offset:32
	ds_bpermute_b32 v178, v19, v18 offset:36
	ds_bpermute_b32 v177, v19, v18 offset:40
	ds_bpermute_b32 v176, v19, v18 offset:44
	ds_bpermute_b32 v175, v19, v18 offset:64
	ds_bpermute_b32 v174, v19, v18 offset:68
	ds_bpermute_b32 v173, v19, v18 offset:72
	ds_bpermute_b32 v172, v19, v18 offset:76
	ds_bpermute_b32 v171, v19, v18 offset:96
	ds_bpermute_b32 v170, v19, v18 offset:100
	ds_bpermute_b32 v169, v19, v18 offset:104
	ds_bpermute_b32 v168, v19, v18 offset:108
	v_lshl_add_u64 v[156:157], v[2:3], 0, s[18:19]
	v_or_b32_e32 v2, 0x22000, v130
	v_mov_b32_e32 v3, v131
	v_lshl_add_u64 v[158:159], s[10:11], 0, v[2:3]
	v_or_b32_e32 v2, 0x16000, v130
	v_lshl_add_u64 v[2:3], s[10:11], 0, v[2:3]
	v_lshl_add_u64 v[160:161], v[2:3], 0, s[18:19]
	v_or_b32_e32 v2, 0x20000, v130
	v_mov_b32_e32 v3, v131
	v_add_u32_e32 v187, v4, v1
	v_lshl_add_u64 v[162:163], s[10:11], 0, v[2:3]
	s_mov_b64 s[42:43], s[10:11]
	s_mov_b64 s[10:11], 0
	s_movk_i32 s13, 0x3000
	s_waitcnt lgkmcnt(14)
	v_xor_b32_e32 v63, 0x80000000, v43
	v_xor_b32_e32 v62, 0x80000000, v40
	v_xor_b32_e32 v61, 0x80000000, v41
	v_xor_b32_e32 v60, 0x80000000, v38
	v_xor_b32_e32 v59, 0x80000000, v39
	v_xor_b32_e32 v58, 0x80000000, v36
	v_xor_b32_e32 v57, 0x80000000, v37
	v_xor_b32_e32 v56, 0x80000000, v34
	v_xor_b32_e32 v55, 0x80000000, v35
	v_xor_b32_e32 v54, 0x80000000, v32
	v_xor_b32_e32 v53, 0x80000000, v33
	v_add_u32_e32 v186, v5, v0
	v_xor_b32_e32 v52, 0x80000000, v46
	v_xor_b32_e32 v51, 0x80000000, v47
	v_xor_b32_e32 v50, 0x80000000, v42
	v_xor_b32_e32 v49, 0x80000000, v45
	v_xor_b32_e32 v48, 0x80000000, v44
	v_mov_b32_e32 v0, v131
	v_mov_b32_e32 v1, v131
	v_mov_b32_e32 v2, v131
	v_mov_b32_e32 v4, v131
	v_mov_b32_e32 v5, v131
	v_mov_b32_e32 v6, v131
	v_mov_b32_e32 v7, v131
	v_mov_b32_e32 v8, v131
	v_mov_b32_e32 v9, v131
	v_mov_b32_e32 v10, v131
	v_mov_b32_e32 v11, v131
	v_mov_b32_e32 v12, v131
	v_mov_b32_e32 v13, v131
	v_mov_b32_e32 v14, v131
	v_mov_b32_e32 v15, v131
	v_mov_b32_e32 v16, v131
	v_mov_b32_e32 v17, v131
	v_mov_b32_e32 v18, v131
	v_mov_b32_e32 v19, v131
	v_mov_b32_e32 v20, v131
	v_mov_b32_e32 v21, v131
	v_mov_b32_e32 v22, v131
	v_mov_b32_e32 v23, v131
	v_mov_b32_e32 v24, v131
	v_mov_b32_e32 v25, v131
	v_mov_b32_e32 v26, v131
	v_mov_b32_e32 v27, v131
	v_mov_b32_e32 v28, v131
	v_mov_b32_e32 v29, v131
	v_mov_b32_e32 v30, v131
	v_mov_b32_e32 v31, v131
	v_add_u32_e32 v131, 0x800, v187
	v_or_b32_e32 v132, 0x80, v130
	v_or_b32_e32 v136, 0x2080, v130
	v_or_b32_e32 v140, 0x4080, v130
	v_or_b32_e32 v144, 0x6080, v130
	v_or_b32_e32 v148, 0x10080, v130
	v_or_b32_e32 v152, 0x12080, v130
	v_or_b32_e32 v156, 0x14080, v130
	v_or_b32_e32 v160, 0x16080, v130
	v_or_b32_e32 v162, 0x20000, v130
	v_or_b32_e32 v158, 0x22000, v130
	v_or_b32_e32 v154, 0x24000, v130
	v_or_b32_e32 v150, 0x26000, v130
	v_or_b32_e32 v146, 0x30000, v130
	v_or_b32_e32 v142, 0x32000, v130
	v_or_b32_e32 v138, 0x34000, v130
	v_or_b32_e32 v134, 0x36000, v130
	s_waitcnt lgkmcnt(0)
	s_barrier
.LBB4_11:
	v_lshl_add_u64 v[66:67], s[8:9], 0, v[128:129]
	v_add_co_u32_e32 v66, vcc, s13, v66
	v_lshl_add_u64 v[64:65], s[0:1], 0, v[128:129]
	s_nop 0
	v_addc_co_u32_e32 v67, vcc, 0, v67, vcc
	v_add_co_u32_e32 v64, vcc, s13, v64
	s_and_b32 s14, s15, 1
	s_nop 0
	v_addc_co_u32_e32 v65, vcc, 0, v65, vcc
	global_load_dwordx4 v[112:115], v[66:67], off offset:-4096
	global_load_dwordx4 v[116:119], v[66:67], off
	global_load_dwordx4 v[120:123], v[64:65], off offset:-4096
	global_load_dwordx4 v[124:127], v[64:65], off
	s_add_i32 s15, s15, 1
	s_mul_i32 s18, s14, 0x2400
	v_add_u32_e32 v202, s18, v167
	ds_read_b128 v[80:83], v202
	ds_read_b128 v[190:193], v202 offset:32
	ds_read_b128 v[194:197], v202 offset:4608
	ds_read_b128 v[198:201], v202 offset:4640
	s_waitcnt lgkmcnt(3)
	v_mfma_f32_32x32x16_f16 v[64:79], v[108:111], v[80:83], v[48:63]
	s_waitcnt lgkmcnt(1)
	v_mfma_f32_32x32x16_f16 v[80:95], v[108:111], v[194:197], v[48:63]
	v_mfma_f32_32x32x16_f16 v[64:79], v[104:107], v[190:193], v[64:79]
	ds_read_b128 v[190:193], v202 offset:64
	ds_read_b128 v[194:197], v202 offset:96
	s_waitcnt lgkmcnt(2)
	v_mfma_f32_32x32x16_f16 v[80:95], v[104:107], v[198:201], v[80:95]
	s_waitcnt lgkmcnt(1)
	v_mfma_f32_32x32x16_f16 v[64:79], v[100:103], v[190:193], v[64:79]
	ds_read_b128 v[190:193], v202 offset:4672
	ds_read_b128 v[198:201], v202 offset:4704
	s_waitcnt lgkmcnt(1)
	v_mfma_f32_32x32x16_f16 v[80:95], v[100:103], v[190:193], v[80:95]
	v_mfma_f32_32x32x16_f16 v[64:79], v[96:99], v[194:197], v[64:79]
	s_waitcnt lgkmcnt(0)
	v_mfma_f32_32x32x16_f16 v[80:95], v[96:99], v[198:201], v[80:95]
	s_setprio 2
	s_nop 8
	v_exp_f32_e32 v192, v64
	s_nop 0
	v_exp_f32_e32 v80, v80
	v_exp_f32_e32 v193, v65
	v_exp_f32_e32 v81, v81
	v_mul_f32_e32 v64, v192, v183
	v_exp_f32_e32 v66, v66
	global_store_dword v132, v64, s[42:43] offset:-128
	v_mul_f32_e32 v64, v80, v183
	v_exp_f32_e32 v82, v82
	global_store_dword v132, v64, s[42:43]
	v_mul_f32_e32 v190, v193, v182
	v_exp_f32_e32 v67, v67
	global_store_dword v136, v190, s[42:43] offset:-128
	v_mul_f32_e32 v190, v81, v182
	v_exp_f32_e32 v83, v83
	global_store_dword v136, v190, s[42:43]
	v_mul_f32_e32 v190, v66, v181
	global_store_dword v140, v190, s[42:43] offset:-128
	v_mul_f32_e32 v190, v82, v181
	global_store_dword v140, v190, s[42:43]
	v_mul_f32_e32 v190, v67, v180
	global_store_dword v144, v190, s[42:43] offset:-128
	v_mul_f32_e32 v190, v83, v180
	global_store_dword v144, v190, s[42:43]
	v_exp_f32_e32 v190, v68
	v_cvt_pk_f16_f32 v65, v66, v67
	v_cvt_pk_f16_f32 v67, v82, v83
	v_exp_f32_e32 v82, v84
	v_cvt_pk_f16_f32 v66, v80, v81
	v_mul_f32_e32 v68, v190, v179
	global_store_dword v148, v68, s[42:43] offset:-128
	v_exp_f32_e32 v83, v69
	v_mul_f32_e32 v68, v82, v179
	global_store_dword v148, v68, s[42:43]
	v_exp_f32_e32 v80, v85
	v_mul_f32_e32 v81, v83, v178
	global_store_dword v152, v81, s[42:43] offset:-128
	v_exp_f32_e32 v70, v70
	v_mul_f32_e32 v81, v80, v178
	global_store_dword v152, v81, s[42:43]
	v_exp_f32_e32 v81, v86
	v_mul_f32_e32 v84, v70, v177
	global_store_dword v156, v84, s[42:43] offset:-128
	v_exp_f32_e32 v71, v71
	v_mul_f32_e32 v84, v81, v177
	global_store_dword v156, v84, s[42:43]
	v_exp_f32_e32 v84, v87
	v_mul_f32_e32 v85, v71, v176
	global_store_dword v160, v85, s[42:43] offset:-128
	v_mul_f32_e32 v85, v84, v176
	v_cvt_pk_f16_f32 v64, v192, v193
	global_store_dword v160, v85, s[42:43]
	v_cvt_pk_f16_f32 v69, v70, v71
	v_cvt_pk_f16_f32 v68, v190, v83
	v_exp_f32_e32 v72, v72
	v_cvt_pk_f16_f32 v71, v81, v84
	v_cvt_pk_f16_f32 v70, v82, v80
	ds_write2_b64 v187, v[64:65], v[68:69] offset1:2
	ds_write2_b64 v131, v[66:67], v[70:71] offset0:32 offset1:34
	v_exp_f32_e32 v66, v88
	v_mul_f32_e32 v67, v72, v175
	global_store_dword v162, v67, s[42:43]
	v_exp_f32_e32 v67, v73
	v_mul_f32_e32 v68, v66, v175
	global_store_dword v162, v68, s[42:43] offset:128
	v_exp_f32_e32 v68, v89
	v_mul_f32_e32 v69, v67, v174
	global_store_dword v158, v69, s[42:43]
	v_exp_f32_e32 v69, v74
	v_mul_f32_e32 v70, v68, v174
	global_store_dword v158, v70, s[42:43] offset:128
	v_exp_f32_e32 v70, v90
	v_mul_f32_e32 v71, v69, v173
	global_store_dword v154, v71, s[42:43]
	v_exp_f32_e32 v71, v75
	v_mul_f32_e32 v73, v70, v173
	global_store_dword v154, v73, s[42:43] offset:128
	v_exp_f32_e32 v73, v91
	v_mul_f32_e32 v74, v71, v172
	global_store_dword v150, v74, s[42:43]
	v_mul_f32_e32 v74, v73, v172
	global_store_dword v150, v74, s[42:43] offset:128
	v_cvt_pk_f16_f32 v65, v69, v71
	v_exp_f32_e32 v71, v76
	v_cvt_pk_f16_f32 v64, v72, v67
	v_cvt_pk_f16_f32 v67, v70, v73
	v_exp_f32_e32 v70, v92
	v_cvt_pk_f16_f32 v66, v66, v68
	v_mul_f32_e32 v72, v71, v171
	global_store_dword v146, v72, s[42:43]
	v_exp_f32_e32 v72, v77
	v_mul_f32_e32 v73, v70, v171
	global_store_dword v146, v73, s[42:43] offset:128
	v_exp_f32_e32 v73, v93
	v_mul_f32_e32 v74, v72, v170
	global_store_dword v142, v74, s[42:43]
	v_exp_f32_e32 v74, v78
	v_mul_f32_e32 v75, v73, v170
	global_store_dword v142, v75, s[42:43] offset:128
	v_exp_f32_e32 v75, v94
	v_mul_f32_e32 v76, v74, v169
	global_store_dword v138, v76, s[42:43]
	v_exp_f32_e32 v76, v79
	v_mul_f32_e32 v77, v75, v169
	global_store_dword v138, v77, s[42:43] offset:128
	v_exp_f32_e32 v77, v95
	v_mul_f32_e32 v78, v76, v168
	global_store_dword v134, v78, s[42:43]
	v_mul_f32_e32 v78, v77, v168
	global_store_dword v134, v78, s[42:43] offset:128
	v_cvt_pk_f16_f32 v69, v74, v76
	v_cvt_pk_f16_f32 v68, v71, v72
	v_cvt_pk_f16_f32 v71, v75, v77
	v_cvt_pk_f16_f32 v70, v70, v73
	ds_write2_b64 v187, v[64:65], v[68:69] offset0:4 offset1:6
	ds_write2_b64 v131, v[66:67], v[70:71] offset0:36 offset1:38
	s_setprio 0
	ds_read_b64_tr_b16 v[64:65], v186
	ds_read_b64_tr_b16 v[66:67], v186 offset:288
	s_mul_i32 s18, s14, 0x3000
	v_or_b32_e32 v80, s18, v185
	ds_read_b64_tr_b16 v[68:69], v80
	ds_read_b64_tr_b16 v[70:71], v80 offset:768
	ds_read_b64_tr_b16 v[74:75], v80 offset:832
	ds_read_b64_tr_b16 v[72:73], v80 offset:64
	ds_read_b64_tr_b16 v[76:77], v186 offset:1152
	ds_read_b64_tr_b16 v[78:79], v186 offset:1440
	s_waitcnt lgkmcnt(4)
	v_mfma_f32_32x32x16_f16 v[0:15], v[64:67], v[68:71], v[0:15]
	s_waitcnt lgkmcnt(2)
	v_mfma_f32_32x32x16_f16 v[16:31], v[64:67], v[72:75], v[16:31]
	ds_read_b64_tr_b16 v[64:65], v80 offset:3072
	ds_read_b64_tr_b16 v[66:67], v80 offset:3840
	ds_read_b64_tr_b16 v[70:71], v80 offset:3904
	ds_read_b64_tr_b16 v[68:69], v80 offset:3136
	s_waitcnt lgkmcnt(2)
	v_mfma_f32_32x32x16_f16 v[0:15], v[76:79], v[64:67], v[0:15]
	s_waitcnt lgkmcnt(0)
	v_mfma_f32_32x32x16_f16 v[16:31], v[76:79], v[68:71], v[16:31]
	ds_read_b64_tr_b16 v[64:65], v186 offset:2304
	ds_read_b64_tr_b16 v[66:67], v186 offset:2592
	ds_read_b64_tr_b16 v[68:69], v80 offset:6144
	ds_read_b64_tr_b16 v[70:71], v80 offset:6912
	ds_read_b64_tr_b16 v[74:75], v80 offset:6976
	ds_read_b64_tr_b16 v[72:73], v80 offset:6208
	ds_read_b64_tr_b16 v[76:77], v186 offset:3456
	ds_read_b64_tr_b16 v[78:79], v186 offset:3744
	s_waitcnt lgkmcnt(4)
	v_mfma_f32_32x32x16_f16 v[0:15], v[64:67], v[68:71], v[0:15]
	s_waitcnt lgkmcnt(2)
	v_mfma_f32_32x32x16_f16 v[16:31], v[64:67], v[72:75], v[16:31]
	ds_read_b64_tr_b16 v[64:65], v80 offset:9216
	ds_read_b64_tr_b16 v[66:67], v80 offset:9984
	ds_read_b64_tr_b16 v[70:71], v80 offset:10048
	ds_read_b64_tr_b16 v[68:69], v80 offset:9280
	s_waitcnt lgkmcnt(2)
	v_mfma_f32_32x32x16_f16 v[0:15], v[76:79], v[64:67], v[0:15]
	s_waitcnt lgkmcnt(0)
	v_mfma_f32_32x32x16_f16 v[16:31], v[76:79], v[68:71], v[16:31]
	s_xor_b32 s14, s14, 1
	s_mul_i32 s18, s14, 0x3000
	s_mulk_i32 s14, 0x2400
	s_addk_i32 s14, 0x6000
	s_add_u32 s10, s10, 0x100
	s_addc_u32 s11, s11, 0
	s_add_u32 s42, s42, 0x100
	s_addc_u32 s43, s43, 0
	s_add_u32 s8, s8, 0x2000
	s_addc_u32 s9, s9, 0
	s_add_u32 s0, s0, 0x2000
	s_addc_u32 s1, s1, 0
	v_lshl_add_u32 v67, v166, 1, s14
	s_cmpk_eq_i32 s10, 0x1f00
	v_lshl_add_u32 v64, v189, 1, s18
	v_lshl_add_u32 v65, v188, 1, s18
	v_lshl_add_u32 v66, v165, 1, s14
	s_waitcnt vmcnt(35)
	ds_write_b128 v67, v[112:115]
	s_waitcnt vmcnt(34)
	ds_write_b128 v66, v[116:119]
	s_waitcnt vmcnt(33)
	ds_write_b128 v65, v[120:123]
	s_waitcnt vmcnt(32)
	ds_write_b128 v64, v[124:127]
	s_waitcnt lgkmcnt(0)
	s_barrier
	s_cbranch_scc0 .LBB4_11
	s_lshl_b64 s[0:1], s[16:17], 13
	s_add_u32 s0, s4, s0
	s_addc_u32 s1, s5, s1
	v_xor_b32_e32 v52, 0x80000000, v34
	v_xor_b32_e32 v51, 0x80000000, v35
	v_xor_b32_e32 v50, 0x80000000, v32
	v_xor_b32_e32 v49, 0x80000000, v33
	ds_read_b128 v[32:35], v167 offset:9216
	v_xor_b32_e32 v59, 0x80000000, v43
	v_xor_b32_e32 v58, 0x80000000, v40
	v_xor_b32_e32 v57, 0x80000000, v41
	v_xor_b32_e32 v56, 0x80000000, v38
	v_xor_b32_e32 v55, 0x80000000, v39
	v_xor_b32_e32 v54, 0x80000000, v36
	v_xor_b32_e32 v53, 0x80000000, v37
	v_xor_b32_e32 v48, 0x80000000, v46
	v_xor_b32_e32 v47, 0x80000000, v47
	v_xor_b32_e32 v46, 0x80000000, v42
	v_xor_b32_e32 v45, 0x80000000, v45
	v_xor_b32_e32 v44, 0x80000000, v44
	ds_read_b128 v[36:39], v167 offset:9248
	s_add_u32 s0, s0, 0x1f00
	s_waitcnt lgkmcnt(1)
	v_mfma_f32_32x32x16_f16 v[60:75], v[108:111], v[32:35], v[44:59]
	ds_read_b128 v[32:35], v167 offset:13824
	ds_read_b128 v[40:43], v167 offset:13856
	s_addc_u32 s1, s1, 0
	s_waitcnt lgkmcnt(1)
	v_mfma_f32_32x32x16_f16 v[44:59], v[108:111], v[32:35], v[44:59]
	v_mfma_f32_32x32x16_f16 v[60:75], v[104:107], v[36:39], v[60:75]
	ds_read_b128 v[32:35], v167 offset:9280
	ds_read_b128 v[36:39], v167 offset:9312
	s_waitcnt lgkmcnt(2)
	v_mfma_f32_32x32x16_f16 v[44:59], v[104:107], v[40:43], v[44:59]
	s_waitcnt lgkmcnt(1)
	v_mfma_f32_32x32x16_f16 v[60:75], v[100:103], v[32:35], v[60:75]
	ds_read_b128 v[32:35], v167 offset:13888
	ds_read_b128 v[40:43], v167 offset:13920
	s_waitcnt lgkmcnt(1)
	v_mfma_f32_32x32x16_f16 v[44:59], v[100:103], v[32:35], v[44:59]
	v_mfma_f32_32x32x16_f16 v[60:75], v[96:99], v[36:39], v[60:75]
	s_waitcnt lgkmcnt(0)
	v_mfma_f32_32x32x16_f16 v[44:59], v[96:99], v[40:43], v[44:59]
	s_setprio 2
	s_nop 8
	v_exp_f32_e32 v32, v60
	s_nop 0
	v_exp_f32_e32 v34, v44
	v_exp_f32_e32 v35, v61
	v_or_b32_e32 v37, 0x2000, v130
	v_mul_f32_e32 v33, v32, v183
	v_mul_f32_e32 v36, v34, v183
	global_store_dword v130, v33, s[0:1]
	global_store_dword v130, v36, s[0:1] offset:128
	v_exp_f32_e32 v36, v45
	v_mul_f32_e32 v33, v35, v182
	global_store_dword v37, v33, s[0:1]
	v_exp_f32_e32 v33, v62
	v_mul_f32_e32 v38, v36, v182
	global_store_dword v37, v38, s[0:1] offset:128
	v_exp_f32_e32 v37, v46
	v_mul_f32_e32 v38, v33, v181
	v_or_b32_e32 v39, 0x4000, v130
	global_store_dword v39, v38, s[0:1]
	v_exp_f32_e32 v38, v63
	v_mul_f32_e32 v40, v37, v181
	global_store_dword v39, v40, s[0:1] offset:128
	v_exp_f32_e32 v39, v47
	v_mul_f32_e32 v40, v38, v180
	v_cvt_pk_f16_f32 v33, v33, v38
	v_exp_f32_e32 v38, v64
	v_or_b32_e32 v41, 0x6000, v130
	global_store_dword v41, v40, s[0:1]
	v_mul_f32_e32 v40, v39, v180
	global_store_dword v41, v40, s[0:1] offset:128
	v_cvt_pk_f16_f32 v32, v32, v35
	v_cvt_pk_f16_f32 v35, v37, v39
	v_cvt_pk_f16_f32 v34, v34, v36
	v_exp_f32_e32 v40, v48
	v_mul_f32_e32 v36, v38, v179
	v_or_b32_e32 v37, 0x10000, v130
	global_store_dword v37, v36, s[0:1]
	v_exp_f32_e32 v36, v65
	v_exp_f32_e32 v41, v49
	v_mul_f32_e32 v39, v40, v179
	global_store_dword v37, v39, s[0:1] offset:128
	v_mul_f32_e32 v37, v36, v178
	v_or_b32_e32 v39, 0x12000, v130
	global_store_dword v39, v37, s[0:1]
	v_exp_f32_e32 v37, v66
	v_mul_f32_e32 v42, v41, v178
	global_store_dword v39, v42, s[0:1] offset:128
	v_exp_f32_e32 v39, v50
	v_mul_f32_e32 v42, v37, v177
	v_or_b32_e32 v43, 0x14000, v130
	global_store_dword v43, v42, s[0:1]
	v_exp_f32_e32 v42, v67
	v_mul_f32_e32 v44, v39, v177
	global_store_dword v43, v44, s[0:1] offset:128
	v_exp_f32_e32 v43, v51
	v_cvt_pk_f16_f32 v37, v37, v42
	v_cvt_pk_f16_f32 v36, v38, v36
	v_cvt_pk_f16_f32 v38, v40, v41
	v_cvt_pk_f16_f32 v39, v39, v43
	ds_write2_b64 v187, v[32:33], v[36:37] offset1:2
	v_exp_f32_e32 v32, v68
	v_add_u32_e32 v40, 0x800, v187
	ds_write2_b64 v40, v[34:35], v[38:39] offset0:32 offset1:34
	v_exp_f32_e32 v34, v52
	v_exp_f32_e32 v36, v69
	v_exp_f32_e32 v37, v53
	v_mul_f32_e32 v33, v32, v175
	v_or_b32_e32 v35, 0x20000, v130
	global_store_dword v35, v33, s[0:1]
	v_mul_f32_e32 v33, v34, v175
	global_store_dword v35, v33, s[0:1] offset:128
	v_mul_f32_e32 v33, v36, v174
	v_or_b32_e32 v35, 0x22000, v130
	global_store_dword v35, v33, s[0:1]
	v_exp_f32_e32 v33, v70
	v_mul_f32_e32 v38, v37, v174
	global_store_dword v35, v38, s[0:1] offset:128
	v_exp_f32_e32 v35, v54
	v_mul_f32_e32 v38, v33, v173
	v_or_b32_e32 v39, 0x24000, v130
	global_store_dword v39, v38, s[0:1]
	v_exp_f32_e32 v38, v71
	v_mul_f32_e32 v41, v35, v173
	global_store_dword v39, v41, s[0:1] offset:128
	v_exp_f32_e32 v39, v55
	v_mul_f32_e32 v44, v42, v176
	v_mul_f32_e32 v41, v38, v172
	v_or_b32_e32 v42, 0x26000, v130
	v_cvt_pk_f16_f32 v32, v32, v36
	v_exp_f32_e32 v36, v72
	global_store_dword v42, v41, s[0:1]
	v_mul_f32_e32 v41, v39, v172
	v_cvt_pk_f16_f32 v33, v33, v38
	v_exp_f32_e32 v38, v56
	global_store_dword v42, v41, s[0:1] offset:128
	v_exp_f32_e32 v41, v73
	v_exp_f32_e32 v42, v57
	v_cvt_pk_f16_f32 v35, v35, v39
	v_cvt_pk_f16_f32 v34, v34, v37
	v_mul_f32_e32 v37, v36, v171
	v_or_b32_e32 v39, 0x30000, v130
	global_store_dword v39, v37, s[0:1]
	v_mul_f32_e32 v37, v38, v171
	v_or_b32_e32 v45, 0x16000, v130
	global_store_dword v39, v37, s[0:1] offset:128
	v_mul_f32_e32 v37, v41, v170
	v_or_b32_e32 v39, 0x32000, v130
	global_store_dword v45, v44, s[0:1]
	v_mul_f32_e32 v44, v43, v176
	global_store_dword v39, v37, s[0:1]
	v_exp_f32_e32 v37, v74
	v_mul_f32_e32 v43, v42, v170
	global_store_dword v39, v43, s[0:1] offset:128
	v_exp_f32_e32 v39, v58
	global_store_dword v45, v44, s[0:1] offset:128
	v_mul_f32_e32 v43, v37, v169
	v_or_b32_e32 v44, 0x34000, v130
	global_store_dword v44, v43, s[0:1]
	v_exp_f32_e32 v43, v75
	v_mul_f32_e32 v45, v39, v169
	global_store_dword v44, v45, s[0:1] offset:128
	v_exp_f32_e32 v44, v59
	v_mul_f32_e32 v45, v43, v168
	v_or_b32_e32 v46, 0x36000, v130
	global_store_dword v46, v45, s[0:1]
	v_mul_f32_e32 v45, v44, v168
	v_cvt_pk_f16_f32 v37, v37, v43
	v_cvt_pk_f16_f32 v36, v36, v41
	global_store_dword v46, v45, s[0:1] offset:128
	v_cvt_pk_f16_f32 v39, v39, v44
	v_cvt_pk_f16_f32 v38, v38, v42
	ds_write2_b64 v187, v[32:33], v[36:37] offset0:4 offset1:6
	ds_write2_b64 v40, v[34:35], v[38:39] offset0:36 offset1:38
	s_setprio 0
	ds_read_b64_tr_b16 v[32:33], v186
	ds_read_b64_tr_b16 v[34:35], v186 offset:288
	ds_read_b64_tr_b16 v[36:37], v185 offset:12288
	ds_read_b64_tr_b16 v[38:39], v185 offset:13056
	ds_read_b64_tr_b16 v[42:43], v185 offset:13120
	ds_read_b64_tr_b16 v[40:41], v185 offset:12352
	ds_read_b64_tr_b16 v[44:45], v186 offset:1152
	ds_read_b64_tr_b16 v[46:47], v186 offset:1440
	s_waitcnt lgkmcnt(4)
	v_mfma_f32_32x32x16_f16 v[0:15], v[32:35], v[36:39], v[0:15]
	s_waitcnt lgkmcnt(2)
	v_mfma_f32_32x32x16_f16 v[16:31], v[32:35], v[40:43], v[16:31]
	ds_read_b64_tr_b16 v[32:33], v185 offset:15360
	ds_read_b64_tr_b16 v[34:35], v185 offset:16128
	ds_read_b64_tr_b16 v[38:39], v185 offset:16192
	ds_read_b64_tr_b16 v[36:37], v185 offset:15424
	s_waitcnt lgkmcnt(2)
	v_mfma_f32_32x32x16_f16 v[0:15], v[44:47], v[32:35], v[0:15]
	s_waitcnt lgkmcnt(0)
	v_mfma_f32_32x32x16_f16 v[16:31], v[44:47], v[36:39], v[16:31]
	ds_read_b64_tr_b16 v[32:33], v186 offset:2304
	ds_read_b64_tr_b16 v[34:35], v186 offset:2592
	ds_read_b64_tr_b16 v[36:37], v185 offset:18432
	ds_read_b64_tr_b16 v[38:39], v185 offset:19200
	ds_read_b64_tr_b16 v[42:43], v185 offset:19264
	ds_read_b64_tr_b16 v[40:41], v185 offset:18496
	ds_read_b64_tr_b16 v[44:45], v186 offset:3456
	ds_read_b64_tr_b16 v[46:47], v186 offset:3744
	s_waitcnt lgkmcnt(4)
	v_mfma_f32_32x32x16_f16 v[0:15], v[32:35], v[36:39], v[0:15]
	s_waitcnt lgkmcnt(2)
	v_mfma_f32_32x32x16_f16 v[16:31], v[32:35], v[40:43], v[16:31]
	ds_read_b64_tr_b16 v[32:33], v185 offset:21504
	ds_read_b64_tr_b16 v[34:35], v185 offset:22272
	ds_read_b64_tr_b16 v[38:39], v185 offset:22336
	ds_read_b64_tr_b16 v[36:37], v185 offset:21568
	s_waitcnt lgkmcnt(2)
	v_mfma_f32_32x32x16_f16 v[0:15], v[44:47], v[32:35], v[0:15]
	s_waitcnt lgkmcnt(0)
	v_mfma_f32_32x32x16_f16 v[16:31], v[44:47], v[36:39], v[16:31]
	s_lshl_b32 s0, s2, 3
	s_and_b32 s0, s0, 0x7ffff800
	s_add_i32 s3, s3, s0
	s_lshl_b32 s0, s12, 7
	s_and_b32 s0, s0, 0x780
	s_add_u32 s0, s6, s0
	v_mov_b32_e32 v35, 0
	v_or_b32_e32 v32, s3, v184
	s_addc_u32 s1, s7, 0
	v_lshlrev_b32_e32 v34, 1, v164
	v_mov_b32_e32 v33, v35
	v_lshl_add_u64 v[36:37], s[0:1], 0, v[34:35]
	v_lshlrev_b64 v[38:39], 11, v[32:33]
	v_fma_mixlo_f16 v0, v0, v183, 0
	v_lshl_add_u64 v[38:39], v[36:37], 0, v[38:39]
	s_waitcnt vmcnt(63) expcnt(7) lgkmcnt(15)
	s_barrier
	global_store_short v[38:39], v0, off
	v_fma_mixlo_f16 v0, v16, v183, 0
	v_or_b32_e32 v34, 1, v32
	global_store_short v[38:39], v0, off offset:64
	v_lshlrev_b64 v[38:39], 11, v[34:35]
	v_fma_mixlo_f16 v16, v1, v182, 0
	v_lshl_add_u64 v[0:1], v[36:37], 0, v[38:39]
	global_store_short v[0:1], v16, off
	v_fma_mixlo_f16 v16, v17, v182, 0
	v_or_b32_e32 v34, 2, v32
	global_store_short v[0:1], v16, off offset:64
	v_lshlrev_b64 v[0:1], 11, v[34:35]
	v_fma_mixlo_f16 v2, v2, v181, 0
	v_lshl_add_u64 v[0:1], v[36:37], 0, v[0:1]
	global_store_short v[0:1], v2, off
	v_fma_mixlo_f16 v2, v18, v181, 0
	v_or_b32_e32 v34, 3, v32
	global_store_short v[0:1], v2, off offset:64
	v_lshlrev_b64 v[0:1], 11, v[34:35]
	v_fma_mixlo_f16 v2, v3, v180, 0
	v_lshl_add_u64 v[0:1], v[36:37], 0, v[0:1]
	global_store_short v[0:1], v2, off
	v_fma_mixlo_f16 v2, v19, v180, 0
	v_or_b32_e32 v34, 8, v32
	global_store_short v[0:1], v2, off offset:64
	v_lshlrev_b64 v[0:1], 11, v[34:35]
	v_fma_mixlo_f16 v2, v4, v179, 0
	v_lshl_add_u64 v[0:1], v[36:37], 0, v[0:1]
	global_store_short v[0:1], v2, off
	v_fma_mixlo_f16 v2, v20, v179, 0
	v_or_b32_e32 v34, 9, v32
	global_store_short v[0:1], v2, off offset:64
	v_lshlrev_b64 v[0:1], 11, v[34:35]
	v_fma_mixlo_f16 v2, v5, v178, 0
	v_lshl_add_u64 v[0:1], v[36:37], 0, v[0:1]
	global_store_short v[0:1], v2, off
	v_fma_mixlo_f16 v2, v21, v178, 0
	v_or_b32_e32 v34, 10, v32
	global_store_short v[0:1], v2, off offset:64
	v_lshlrev_b64 v[0:1], 11, v[34:35]
	v_fma_mixlo_f16 v2, v6, v177, 0
	v_lshl_add_u64 v[0:1], v[36:37], 0, v[0:1]
	global_store_short v[0:1], v2, off
	v_fma_mixlo_f16 v2, v22, v177, 0
	v_or_b32_e32 v34, 11, v32
	global_store_short v[0:1], v2, off offset:64
	v_lshlrev_b64 v[0:1], 11, v[34:35]
	v_fma_mixlo_f16 v2, v7, v176, 0
	v_lshl_add_u64 v[0:1], v[36:37], 0, v[0:1]
	global_store_short v[0:1], v2, off
	v_fma_mixlo_f16 v2, v23, v176, 0
	v_or_b32_e32 v34, 16, v32
	global_store_short v[0:1], v2, off offset:64
	v_lshlrev_b64 v[0:1], 11, v[34:35]
	v_fma_mixlo_f16 v2, v8, v175, 0
	v_lshl_add_u64 v[0:1], v[36:37], 0, v[0:1]
	global_store_short v[0:1], v2, off
	v_fma_mixlo_f16 v2, v24, v175, 0
	v_or_b32_e32 v34, 17, v32
	global_store_short v[0:1], v2, off offset:64
	v_lshlrev_b64 v[0:1], 11, v[34:35]
	v_fma_mixlo_f16 v2, v9, v174, 0
	v_lshl_add_u64 v[0:1], v[36:37], 0, v[0:1]
	global_store_short v[0:1], v2, off
	v_fma_mixlo_f16 v2, v25, v174, 0
	v_or_b32_e32 v34, 18, v32
	global_store_short v[0:1], v2, off offset:64
	v_lshlrev_b64 v[0:1], 11, v[34:35]
	v_fma_mixlo_f16 v2, v10, v173, 0
	v_lshl_add_u64 v[0:1], v[36:37], 0, v[0:1]
	global_store_short v[0:1], v2, off
	v_fma_mixlo_f16 v2, v26, v173, 0
	v_or_b32_e32 v34, 19, v32
	global_store_short v[0:1], v2, off offset:64
	v_lshlrev_b64 v[0:1], 11, v[34:35]
	v_fma_mixlo_f16 v2, v11, v172, 0
	v_lshl_add_u64 v[0:1], v[36:37], 0, v[0:1]
	global_store_short v[0:1], v2, off
	v_fma_mixlo_f16 v2, v27, v172, 0
	v_or_b32_e32 v34, 24, v32
	global_store_short v[0:1], v2, off offset:64
	v_lshlrev_b64 v[0:1], 11, v[34:35]
	v_fma_mixlo_f16 v2, v12, v171, 0
	v_lshl_add_u64 v[0:1], v[36:37], 0, v[0:1]
	global_store_short v[0:1], v2, off
	v_fma_mixlo_f16 v2, v28, v171, 0
	v_or_b32_e32 v34, 25, v32
	global_store_short v[0:1], v2, off offset:64
	v_lshlrev_b64 v[0:1], 11, v[34:35]
	v_fma_mixlo_f16 v2, v13, v170, 0
	v_lshl_add_u64 v[0:1], v[36:37], 0, v[0:1]
	global_store_short v[0:1], v2, off
	v_fma_mixlo_f16 v2, v29, v170, 0
	v_or_b32_e32 v34, 26, v32
	global_store_short v[0:1], v2, off offset:64
	v_lshlrev_b64 v[0:1], 11, v[34:35]
	v_fma_mixlo_f16 v2, v14, v169, 0
	v_lshl_add_u64 v[0:1], v[36:37], 0, v[0:1]
	global_store_short v[0:1], v2, off
	v_fma_mixlo_f16 v2, v30, v169, 0
	v_or_b32_e32 v34, 27, v32
	global_store_short v[0:1], v2, off offset:64
	v_lshlrev_b64 v[0:1], 11, v[34:35]
	v_fma_mixlo_f16 v2, v15, v168, 0
	v_lshl_add_u64 v[0:1], v[36:37], 0, v[0:1]
	global_store_short v[0:1], v2, off
	v_fma_mixlo_f16 v2, v31, v168, 0
	global_store_short v[0:1], v2, off offset:64
	s_endpgm
	.p2alignl 8, 3212836864
